# conversion queue split into 8 sub-queues with their own counters (items interleaved, workgroup pair -> sub-queue) to cut same-address atomic contention; 4 items per claim
# speedup vs baseline: 1.0232x; 1.0232x over previous
; #define RI_NEXT(D_) do { if (q.cnt == 8) { int b_ = 0; if (F.lane == 0) b_ = (int)__hip_atomic_fetch_add(qctr, 8u, __ATOMIC_RELAXED, __HIP_MEMORY_SCOPE_AGENT); q.base = __builtin_amdgcn_readfirstlane(b_); q.cnt = 0; } \
;         D_ = decode_item(KA, F.ws, kind, q.base + q.cnt); ++q.cnt; } while (0)
; DI void run_items1(Frame& F, int kind, int quota, QState& q) {
;     ...
;     if (quota == 0) return;
;     TItem d; RI_NEXT(d); if (!d.valid) return;
; DI void phase_attn(Frame& F, int l) {
;     ...
;     QState cq; cq.base = 0; cq.cnt = 8;
;     constexpr int SLOT_ITEMS = 3;
;     if (F.bid & 1) { __syncthreads(); run_items1(F, 1 + l, SLOT_ITEMS, cq); }
.LBB0_398:
	v_readlane_b32 s8, v255, 14
	v_readlane_b32 s4, v253, 8
	s_lshl_b32 s58, s8, 6
	v_readlane_b32 s6, v253, 10
	v_readlane_b32 s7, v253, 11
	s_lshl_b64 s[0:1], s[58:59], 2
	s_mov_b64 s[2:3], s[6:7]
	s_add_u32 s0, s2, s0
	s_addc_u32 s1, s3, s1
	v_readlane_b32 s9, v255, 15
	s_add_u32 s12, s0, 0x8100
	s_addc_u32 s13, s1, 0
	v_readlane_b32 s100, v253, 29
	s_lshr_b32 s100, s100, 1
	s_and_b32 s100, s100, 7
	s_lshl_b32 s0, s100, 8
	s_mul_i32 s1, s8, 0x700
	s_add_i32 s0, s0, s1
	s_add_i32 s0, s0, 0xb00
	s_add_u32 s12, s12, s0
	s_addc_u32 s13, s13, 0
	s_lshl_b64 s[0:1], s[8:9], 25
	v_writelane_b32 v255, s0, 16
	s_lshl_b64 s[62:63], s[8:9], 5
	s_lshl_b32 s2, s8, 20
	v_writelane_b32 v255, s1, 17
	s_mov_b32 s3, s59
	v_readlane_b32 s0, v253, 33
	v_writelane_b32 v255, s2, 18
	s_add_u32 s76, s0, s2
	v_readlane_b32 s0, v253, 34
	v_writelane_b32 v255, s3, 19
	s_addc_u32 s77, s0, 0
	s_lshl_b64 s[20:21], s[8:9], 21
	s_lshl_b64 s[0:1], s[8:9], 20
	v_readlane_b32 s2, v253, 35
	s_add_u32 s22, s2, s0
	v_readlane_b32 s2, v253, 36
	s_addc_u32 s23, s2, s1
	v_readlane_b32 s2, v253, 37
	s_add_u32 s24, s2, s0
	v_readlane_b32 s0, v253, 38
	s_addc_u32 s25, s0, s1
	s_lshl_b64 s[26:27], s[8:9], 24
	v_readlane_b32 s0, v253, 39
	s_add_u32 s14, s0, s44
	v_readlane_b32 s0, v253, 40
	s_addc_u32 s15, s0, s45
	s_mov_b32 s0, -1
	s_mov_b32 s95, 0
	v_mbcnt_lo_u32_b32 v0, s0, 0
	v_mbcnt_hi_u32_b32 v186, s0, v0
	v_readlane_b32 s0, v253, 29
	s_mov_b32 s51, s0
	s_mov_b64 s[30:31], s[70:71]
	s_bitcmp0_b32 s51, 0
	s_mov_b32 s63, 4
	v_readlane_b32 s5, v253, 9
	v_readlane_b32 s1, v253, 30
	s_cbranch_scc1 .LBB0_472
	s_mov_b64 s[6:7], s[70:71]
	v_mov_b32_e32 v0, 0
	v_cmp_eq_u32_e64 s[4:5], 0, v186
	s_waitcnt vmcnt(63) expcnt(7) lgkmcnt(15)
	s_barrier
	s_and_saveexec_b64 s[2:3], s[4:5]
	s_cbranch_execz .LBB0_403
	s_mov_b64 s[10:11], exec
	v_mbcnt_lo_u32_b32 v0, s10, 0
	v_mbcnt_hi_u32_b32 v0, s11, v0
	v_cmp_eq_u32_e32 vcc, 0, v0
	s_and_saveexec_b64 s[8:9], vcc
	s_cbranch_execz .LBB0_402
	s_bcnt1_i32_b64 s0, s[10:11]
	s_lshl_b32 s0, s0, 2
	v_mov_b32_e32 v2, s0
	global_atomic_add v2, v1, v2, s[12:13] sc0

; #define RI_NEXT(D_) do { if (q.cnt == 8) { int b_ = 0; if (F.lane == 0) b_ = (int)__hip_atomic_fetch_add(qctr, 8u, __ATOMIC_RELAXED, __HIP_MEMORY_SCOPE_AGENT); q.base = __builtin_amdgcn_readfirstlane(b_); q.cnt = 0; } \
;         D_ = decode_item(KA, F.ws, kind, q.base + q.cnt); ++q.cnt; } while (0)
; DI TItem decode_item(kptr_t KA, unsigned char* ws, int kind, int it) {
;     TItem d; d.valid = it < (kind == 0 ? DEPTH * IT_SMALL : IT_EXP); if (!d.valid) it = 0;
; DI void run_items1(Frame& F, int kind, int quota, QState& q) {
;     ...
;     if (quota == 0) return;
;     TItem d; RI_NEXT(d); if (!d.valid) return;
.LBB0_403:
	s_or_b64 exec, exec, s[2:3]
	v_readfirstlane_b32 s95, v0
	s_lshl_b32 s101, s95, 3
	s_or_b32 s101, s101, s100
	s_cmpk_lt_i32 s101, 0x6000
	s_cselect_b64 s[2:3], -1, 0
	s_and_b64 s[0:1], s[2:3], exec
	s_cselect_b32 s36, s101, 0
	s_add_i32 s0, s36, 0x680
	s_cmpk_gt_i32 s36, 0xfd7f
	s_mov_b64 s[18:19], -1
	s_cbranch_scc0 .LBB0_424
	s_mov_b64 s[34:35], -1
	s_cmpk_gt_u32 s0, 0x47f
	s_mov_b64 s[8:9], -1
	s_cbranch_scc0 .LBB0_421
	s_cmpk_gt_u32 s0, 0x4ff
	s_cbranch_scc0 .LBB0_418
	s_cmpk_gt_u32 s0, 0x57f
	s_cbranch_scc0 .LBB0_415
	s_cmp_lt_u32 s36, 0xfffff980
	s_cbranch_scc0 .LBB0_412
	s_mov_b64 s[28:29], -1
	s_cmpk_gt_u32 s0, 0x467f
	s_cbranch_scc0 .LBB0_410
	s_add_i32 s1, s36, 0xffffc000
	s_lshr_b32 s58, s1, 8
	s_load_dwordx2 s[8:9], s[6:7], 0xd0
	s_and_b32 s1, s36, 0xff
	s_lshl_b64 s[10:11], s[58:59], 20
	v_readlane_b32 s16, v255, 16
	v_readlane_b32 s17, v255, 17
	s_add_u32 s10, s10, s16
	s_addc_u32 s11, s11, s17
	s_lshl_b64 s[16:17], s[10:11], 2
	s_waitcnt lgkmcnt(0)
	s_add_u32 s16, s8, s16
	s_addc_u32 s17, s9, s17
	v_readlane_b32 s8, v253, 45
	s_add_u32 s10, s8, s10
	v_readlane_b32 s8, v253, 46
	s_addc_u32 s11, s8, s11
	s_mov_b64 s[8:9], 0

; DI TItem decode_item(kptr_t KA, unsigned char* ws, int kind, int it) {
;     TItem d; d.valid = it < (kind == 0 ? DEPTH * IT_SMALL : IT_EXP); if (!d.valid) it = 0;
;     const int l = kind == 0 ? it / IT_SMALL : kind - 1; int r = kind == 0 ? it % IT_SMALL : IT_SMALL + it;
.LBB0_437:
	s_add_i32 s9, s63, s95
	s_lshl_b32 s9, s9, 3
	s_or_b32 s9, s9, s100
	s_cmpk_lt_i32 s9, 0x6000
	s_cselect_b64 s[2:3], -1, 0
	s_and_b64 s[0:1], s[2:3], exec
	s_cselect_b32 s9, s9, 0
	s_add_i32 s0, s9, 0x680
	s_cmpk_gt_i32 s9, 0xfd7f
	s_mov_b64 s[18:19], -1
	s_cbranch_scc0 .LBB0_458
	s_mov_b64 s[16:17], -1
	s_cmpk_gt_u32 s0, 0x47f
	s_cbranch_scc0 .LBB0_455
	s_cmpk_gt_u32 s0, 0x4ff
	s_cbranch_scc0 .LBB0_452
	s_cmpk_gt_u32 s0, 0x57f
	s_cbranch_scc0 .LBB0_449
	s_cmp_lt_u32 s9, 0xfffff980
	s_cbranch_scc0 .LBB0_446
	s_mov_b64 s[56:57], -1
	s_cmpk_gt_u32 s0, 0x467f
	s_cbranch_scc0 .LBB0_444
	s_add_i32 s1, s9, 0xffffc000
	s_lshr_b32 s58, s1, 8
	s_load_dwordx2 s[18:19], s[6:7], 0xd0
	s_and_b32 s1, s9, 0xff
	s_lshl_b64 s[28:29], s[58:59], 20
	v_readlane_b32 s36, v255, 16
	v_readlane_b32 s37, v255, 17
	s_add_u32 s28, s28, s36
	s_addc_u32 s29, s29, s37
	s_lshl_b64 s[36:37], s[28:29], 2
	s_waitcnt lgkmcnt(0)
	s_add_u32 s42, s18, s36
	s_addc_u32 s43, s19, s37
	v_readlane_b32 s18, v253, 45
	s_add_u32 s28, s18, s28
	v_readlane_b32 s18, v253, 46
	s_addc_u32 s29, s18, s29
	s_mov_b64 s[18:19], 0

; DI TItem decode_item(kptr_t KA, unsigned char* ws, int kind, int it) {
;     TItem d; d.valid = it < (kind == 0 ? DEPTH * IT_SMALL : IT_EXP); if (!d.valid) it = 0;
;     const int l = kind == 0 ? it / IT_SMALL : kind - 1; int r = kind == 0 ? it % IT_SMALL : IT_SMALL + it;
.LBB0_575:
	s_add_i32 s8, s63, s95
	s_lshl_b32 s8, s8, 3
	s_or_b32 s8, s8, s100
	s_cmpk_lt_i32 s8, 0x6000
	s_cselect_b64 s[2:3], -1, 0
	s_and_b64 s[0:1], s[2:3], exec
	s_cselect_b32 s36, s8, 0
	s_add_i32 s0, s36, 0x680
	s_cmpk_gt_i32 s36, 0xfd7f
	s_mov_b64 s[18:19], -1
	s_cbranch_scc0 .LBB0_596
	s_mov_b64 s[42:43], -1
	s_cmpk_gt_u32 s0, 0x47f
	s_mov_b64 s[8:9], -1
	s_cbranch_scc0 .LBB0_593
	s_cmpk_gt_u32 s0, 0x4ff
	s_cbranch_scc0 .LBB0_590
	s_cmpk_gt_u32 s0, 0x57f
	s_cbranch_scc0 .LBB0_587
	s_cmp_lt_u32 s36, 0xfffff980
	s_cbranch_scc0 .LBB0_584
	s_mov_b64 s[28:29], -1
	s_cmpk_gt_u32 s0, 0x467f
	s_cbranch_scc0 .LBB0_582
	s_add_i32 s1, s36, 0xffffc000
	s_lshr_b32 s58, s1, 8
	s_load_dwordx2 s[8:9], s[6:7], 0xd0
	s_and_b32 s1, s36, 0xff
	s_lshl_b64 s[10:11], s[58:59], 20
	v_readlane_b32 s16, v255, 16
	v_readlane_b32 s17, v255, 17
	s_add_u32 s10, s10, s16
	s_addc_u32 s11, s11, s17
	s_lshl_b64 s[16:17], s[10:11], 2
	s_waitcnt lgkmcnt(0)
	s_add_u32 s16, s8, s16
	s_addc_u32 s17, s9, s17
	v_readlane_b32 s8, v253, 45
	s_add_u32 s10, s8, s10
	v_readlane_b32 s8, v253, 46
	s_addc_u32 s11, s8, s11
	s_mov_b64 s[8:9], 0

; DI const float* inp(kptr_t k, int i) { return (const float*)k[i]; }
; DI int imap(int n, int H) { return ((n % H) / 128) * 256 + (n / H) * 128 + (n % 128); }
; DI TItem decode_item(kptr_t KA, unsigned char* ws, int kind, int it) {
;     TItem d; d.valid = it < (kind == 0 ? DEPTH * IT_SMALL : IT_EXP); if (!d.valid) it = 0;
;     const int l = kind == 0 ? it / IT_SMALL : kind - 1; int r = kind == 0 ? it % IT_SMALL : IT_SMALL + it;
;     const float* W; unsigned char* WT; int K, N, H = 0; bool f8 = false;
;     int nsub = 0, Kd = 0, kofs = 0;
;     if (r < IT_IN) { W = inp(KA, I_WIN) + (size_t)l * D * INW; K = D; N = INW;
;         WT = ws + WS_WIN + (size_t)l * INW * D; f8 = true; }
;     else if ((r -= IT_IN) < IT_GLU) { W = inp(KA, I_WGLU) + (size_t)l * SW * 1024; WT = ws + WS_WGLU + (size_t)l * 1024 * SW * 2; K = SW; N = 1024; H = 512; }
;     else if ((r -= IT_GLU) < IT_ATT) { W = inp(KA, I_WATTO) + (size_t)l * AW * D; WT = ws + WS_WCAT + (size_t)l * D * D; K = AW; N = D; Kd = D; f8 = true; }
;     else if ((r -= IT_ATT) < IT_SSMO) { W = inp(KA, I_WSSMO) + (size_t)l * SW * D; WT = ws + WS_WCAT + (size_t)l * D * D; K = SW; N = D; Kd = D; kofs = AW; f8 = true; }
;     else if ((r -= IT_SSMO) < IT_OUT) { W = inp(KA, I_WOUT) + (size_t)l * D * D; WT = ws + WS_WOUT + (size_t)l * D * D; K = D; N = D; f8 = true; }
;     else if ((r -= IT_OUT) < NE * IT_W1) { const int e = r / IT_W1; r %= IT_W1; W = inp(KA, I_WEXPIN) + ((size_t)l * NE + e) * D * 2048; WT = ws + WS_W1 + ((size_t)l * NE + e) * 2048 * D; K = D; N = 2048; H = 1024; f8 = true; }
;     else { r -= NE * IT_W1; const int e = r / IT_W2; r %= IT_W2; W = inp(KA, I_WEXPOUT) + ((size_t)l * NE + e) * DFF * D; WT = ws + WS_W2 + ((size_t)l * NE + e) * D * DFF; K = DFF; N = D; f8 = true; }
;     const int nblk = N / 64, kb = r / nblk, nb = r % nblk, n0 = nb * 64;
;     d.W = W; d.WT = WT; d.N = N; d.Kd = Kd ? Kd : K; d.kofs = kofs; d.drow0 = (H ? imap(n0, H) : n0) - nsub; d.k0 = kb * 64; d.n0 = n0; d.f8 = f8;
.LBB0_609:
	s_add_i32 s9, s63, s95
	s_lshl_b32 s9, s9, 3
	s_or_b32 s9, s9, s100
	s_cmpk_lt_i32 s9, 0x6000
	s_cselect_b64 s[2:3], -1, 0
	s_and_b64 s[0:1], s[2:3], exec
	s_cselect_b32 s9, s9, 0
	s_add_i32 s0, s9, 0x680
	s_cmpk_gt_i32 s9, 0xfd7f
	s_mov_b64 s[18:19], -1
	s_cbranch_scc0 .LBB0_630
	s_mov_b64 s[16:17], -1
	s_cmpk_gt_u32 s0, 0x47f
	s_cbranch_scc0 .LBB0_627
	s_cmpk_gt_u32 s0, 0x4ff
	s_cbranch_scc0 .LBB0_624
	s_cmpk_gt_u32 s0, 0x57f
	s_cbranch_scc0 .LBB0_621
	s_cmp_lt_u32 s9, 0xfffff980
	s_cbranch_scc0 .LBB0_618
	s_mov_b64 s[78:79], -1
	s_cmpk_gt_u32 s0, 0x467f
	s_cbranch_scc0 .LBB0_616
	s_add_i32 s1, s9, 0xffffc000
	s_lshr_b32 s58, s1, 8
	s_load_dwordx2 s[18:19], s[6:7], 0xd0
	s_and_b32 s1, s9, 0xff
	s_lshl_b64 s[28:29], s[58:59], 20
	v_readlane_b32 s36, v255, 16
	v_readlane_b32 s37, v255, 17
	s_add_u32 s28, s28, s36
	s_addc_u32 s29, s29, s37
	s_lshl_b64 s[36:37], s[28:29], 2
	s_waitcnt lgkmcnt(0)
	s_add_u32 s56, s18, s36
	s_addc_u32 s57, s19, s37
	v_readlane_b32 s18, v253, 45
	s_add_u32 s28, s18, s28
	v_readlane_b32 s18, v253, 46
	s_addc_u32 s29, s18, s29
	s_mov_b64 s[18:19], 0

; DI const float* inp(kptr_t k, int i) { return (const float*)k[i]; }
; DI int imap(int n, int H) { return ((n % H) / 128) * 256 + (n / H) * 128 + (n % 128); }
; DI TItem decode_item(kptr_t KA, unsigned char* ws, int kind, int it) {
;     TItem d; d.valid = it < (kind == 0 ? DEPTH * IT_SMALL : IT_EXP); if (!d.valid) it = 0;
;     const int l = kind == 0 ? it / IT_SMALL : kind - 1; int r = kind == 0 ? it % IT_SMALL : IT_SMALL + it;
;     const float* W; unsigned char* WT; int K, N, H = 0; bool f8 = false;
;     int nsub = 0, Kd = 0, kofs = 0;
;     if (r < IT_IN) { W = inp(KA, I_WIN) + (size_t)l * D * INW; K = D; N = INW;
;         WT = ws + WS_WIN + (size_t)l * INW * D; f8 = true; }
;     else if ((r -= IT_IN) < IT_GLU) { W = inp(KA, I_WGLU) + (size_t)l * SW * 1024; WT = ws + WS_WGLU + (size_t)l * 1024 * SW * 2; K = SW; N = 1024; H = 512; }
;     else if ((r -= IT_GLU) < IT_ATT) { W = inp(KA, I_WATTO) + (size_t)l * AW * D; WT = ws + WS_WCAT + (size_t)l * D * D; K = AW; N = D; Kd = D; f8 = true; }
;     else if ((r -= IT_ATT) < IT_SSMO) { W = inp(KA, I_WSSMO) + (size_t)l * SW * D; WT = ws + WS_WCAT + (size_t)l * D * D; K = SW; N = D; Kd = D; kofs = AW; f8 = true; }
;     else if ((r -= IT_SSMO) < IT_OUT) { W = inp(KA, I_WOUT) + (size_t)l * D * D; WT = ws + WS_WOUT + (size_t)l * D * D; K = D; N = D; f8 = true; }
;     else if ((r -= IT_OUT) < NE * IT_W1) { const int e = r / IT_W1; r %= IT_W1; W = inp(KA, I_WEXPIN) + ((size_t)l * NE + e) * D * 2048; WT = ws + WS_W1 + ((size_t)l * NE + e) * 2048 * D; K = D; N = 2048; H = 1024; f8 = true; }
;     else { r -= NE * IT_W1; const int e = r / IT_W2; r %= IT_W2; W = inp(KA, I_WEXPOUT) + ((size_t)l * NE + e) * DFF * D; WT = ws + WS_W2 + ((size_t)l * NE + e) * D * DFF; K = DFF; N = D; f8 = true; }
;     const int nblk = N / 64, kb = r / nblk, nb = r % nblk, n0 = nb * 64;
;     d.W = W; d.WT = WT; d.N = N; d.Kd = Kd ? Kd : K; d.kofs = kofs; d.drow0 = (H ? imap(n0, H) : n0) - nsub; d.k0 = kb * 64; d.n0 = n0; d.f8 = f8;
.LBB0_651:
	s_add_i32 s4, s63, s95
	s_lshl_b32 s4, s4, 3
	s_or_b32 s4, s4, s100
	s_cmpk_lt_i32 s4, 0x6000
	s_cselect_b64 s[2:3], -1, 0
	s_and_b64 s[0:1], s[2:3], exec
	s_cselect_b32 s33, s4, 0
	s_add_i32 s0, s33, 0x680
	s_cmpk_gt_i32 s33, 0xfd7f
	s_mov_b64 s[18:19], -1
	s_cbranch_scc0 .LBB0_671
	s_mov_b64 s[8:9], -1
	s_cmpk_gt_u32 s0, 0x47f
	s_cbranch_scc0 .LBB0_668
	s_cmpk_gt_u32 s0, 0x4ff
	s_mov_b64 s[34:35], -1
	s_cbranch_scc0 .LBB0_665
	s_cmpk_gt_u32 s0, 0x57f
	s_cbranch_scc0 .LBB0_663
	s_cmp_lt_u32 s33, 0xfffff980
	s_cbranch_scc0 .LBB0_660
	s_mov_b64 s[28:29], -1
	s_cmpk_gt_u32 s0, 0x467f
	s_mov_b64 s[16:17], -1
	s_cbranch_scc0 .LBB0_658
	s_add_i32 s1, s33, 0xffffc000
	s_lshr_b32 s58, s1, 8
	s_load_dwordx2 s[4:5], s[6:7], 0xd0
	s_and_b32 s1, s33, 0xff
	s_lshl_b64 s[10:11], s[58:59], 20
	v_readlane_b32 s16, v255, 16
	v_readlane_b32 s17, v255, 17
	s_add_u32 s10, s10, s16
	s_addc_u32 s11, s11, s17
	s_lshl_b64 s[16:17], s[10:11], 2
	s_waitcnt lgkmcnt(0)
	s_add_u32 s4, s4, s16
	s_addc_u32 s5, s5, s17
	v_readlane_b32 s16, v253, 45
	s_add_u32 s10, s16, s10
	v_readlane_b32 s16, v253, 46
	s_addc_u32 s11, s16, s11
	s_mov_b64 s[16:17], 0

; DI const float* inp(kptr_t k, int i) { return (const float*)k[i]; }
; DI int imap(int n, int H) { return ((n % H) / 128) * 256 + (n / H) * 128 + (n % 128); }
; DI TItem decode_item(kptr_t KA, unsigned char* ws, int kind, int it) {
;     TItem d; d.valid = it < (kind == 0 ? DEPTH * IT_SMALL : IT_EXP); if (!d.valid) it = 0;
;     const int l = kind == 0 ? it / IT_SMALL : kind - 1; int r = kind == 0 ? it % IT_SMALL : IT_SMALL + it;
;     const float* W; unsigned char* WT; int K, N, H = 0; bool f8 = false;
;     int nsub = 0, Kd = 0, kofs = 0;
;     if (r < IT_IN) { W = inp(KA, I_WIN) + (size_t)l * D * INW; K = D; N = INW;
;         WT = ws + WS_WIN + (size_t)l * INW * D; f8 = true; }
;     else if ((r -= IT_IN) < IT_GLU) { W = inp(KA, I_WGLU) + (size_t)l * SW * 1024; WT = ws + WS_WGLU + (size_t)l * 1024 * SW * 2; K = SW; N = 1024; H = 512; }
;     else if ((r -= IT_GLU) < IT_ATT) { W = inp(KA, I_WATTO) + (size_t)l * AW * D; WT = ws + WS_WCAT + (size_t)l * D * D; K = AW; N = D; Kd = D; f8 = true; }
;     else if ((r -= IT_ATT) < IT_SSMO) { W = inp(KA, I_WSSMO) + (size_t)l * SW * D; WT = ws + WS_WCAT + (size_t)l * D * D; K = SW; N = D; Kd = D; kofs = AW; f8 = true; }
;     else if ((r -= IT_SSMO) < IT_OUT) { W = inp(KA, I_WOUT) + (size_t)l * D * D; WT = ws + WS_WOUT + (size_t)l * D * D; K = D; N = D; f8 = true; }
;     else if ((r -= IT_OUT) < NE * IT_W1) { const int e = r / IT_W1; r %= IT_W1; W = inp(KA, I_WEXPIN) + ((size_t)l * NE + e) * D * 2048; WT = ws + WS_W1 + ((size_t)l * NE + e) * 2048 * D; K = D; N = 2048; H = 1024; f8 = true; }
;     else { r -= NE * IT_W1; const int e = r / IT_W2; r %= IT_W2; W = inp(KA, I_WEXPOUT) + ((size_t)l * NE + e) * DFF * D; WT = ws + WS_W2 + ((size_t)l * NE + e) * D * DFF; K = DFF; N = D; f8 = true; }
;     const int nblk = N / 64, kb = r / nblk, nb = r % nblk, n0 = nb * 64;
;     d.W = W; d.WT = WT; d.N = N; d.Kd = Kd ? Kd : K; d.kofs = kofs; d.drow0 = (H ? imap(n0, H) : n0) - nsub; d.k0 = kb * 64; d.n0 = n0; d.f8 = f8;
.LBB0_684:
	s_xor_b64 s[34:35], s[8:9], -1
	s_add_i32 s2, s63, s95
	s_lshl_b32 s2, s2, 3
	s_or_b32 s2, s2, s100
	s_cmpk_gt_i32 s2, 0x5fff
	s_cselect_b64 s[16:17], -1, 0
	s_cmpk_lt_i32 s2, 0x6000
	s_cselect_b64 s[42:43], -1, 0
	s_and_b64 s[0:1], s[42:43], exec
	s_cselect_b32 s44, s2, 0
	s_add_i32 s1, s44, 0x680
	s_cmpk_gt_i32 s44, 0xfd7f
	s_mov_b64 s[18:19], -1
	s_cbranch_scc0 .LBB0_704
	s_mov_b64 s[8:9], -1
	s_cmpk_gt_u32 s1, 0x47f
	s_cbranch_scc0 .LBB0_701
	s_cmpk_gt_u32 s1, 0x4ff
	s_cbranch_scc0 .LBB0_698
	s_cmpk_gt_u32 s1, 0x57f
	s_mov_b64 s[2:3], -1
	s_cbranch_scc0 .LBB0_696
	s_cmp_lt_u32 s44, 0xfffff980
	s_cbranch_scc0 .LBB0_693
	s_mov_b64 s[36:37], -1
	s_cmpk_gt_u32 s1, 0x467f
	s_cbranch_scc0 .LBB0_691
	s_add_i32 s0, s44, 0xffffc000
	s_lshr_b32 s2, s0, 8
	s_load_dwordx2 s[18:19], s[6:7], 0xd0
	s_mov_b32 s3, s59
	s_and_b32 s39, s44, 0xff
	s_lshl_b64 s[2:3], s[2:3], 20
	v_readlane_b32 s28, v255, 16
	v_readlane_b32 s29, v255, 17
	s_add_u32 s2, s2, s28
	s_addc_u32 s3, s3, s29
	s_lshl_b64 s[28:29], s[2:3], 2
	s_waitcnt lgkmcnt(0)
	s_add_u32 s56, s18, s28
	s_addc_u32 s57, s19, s29
	v_readlane_b32 s0, v253, 45
	s_add_u32 s28, s0, s2
	v_readlane_b32 s0, v253, 46
	s_addc_u32 s29, s0, s3
	s_mov_b64 s[2:3], 0
